# split-phase grid barrier 1: workgroups arrive right after the adaLN partial sums and wait only after the phase-0 weight conversions (flag barrier at all sites)
# speedup vs baseline: 1.0114x; 1.0114x over previous
; __device__ __forceinline__ unsigned xb_add(unsigned* p, unsigned v) { return __hip_atomic_fetch_add(p, v, __ATOMIC_RELAXED, __HIP_MEMORY_SCOPE_AGENT); }
; __device__ __forceinline__ void xcd_barrier(const XcdBarrier& b, const int wave) {
;     asm volatile("s_waitcnt vmcnt(0)" ::: "memory");
;     __syncthreads();
;     if (phase_tid(wave) == 0) {
;         unsigned* bar = b.bar;
;         __builtin_amdgcn_s_waitcnt(0);
;         unsigned nloc = b.st[0], nx = b.st[1];
;         if (nloc == 0u) { xcd_barrier_complete(bar, b.x, nloc, nx); b.st[0] = nloc; b.st[1] = nx; }
;         const unsigned old = xb_add(&bar[XB_XSUB(b.x)], 1u);
;         const unsigned gen = old / nloc;
;         if (old + 1u == (gen + 1u) * nloc) {
;             __builtin_amdgcn_fence(__ATOMIC_RELEASE, "agent");
;             asm volatile("s_waitcnt vmcnt(0)" ::: "memory");
;             const unsigned og = xb_add(&bar[XB_TOP], 1u);
;             const unsigned tg = og / nx;
;             if (og + 1u == (tg + 1u) * nx) xb_add(&bar[XB_TOPGEN], 1u);
; __device__ __forceinline__ void phase0(const Params& p, LAS unsigned char* lds, const int wave) {
;     ...
;     }
;     const int gw = bid * NWAVES + wv, GW = gridDim.x * NWAVES;
.LBB0_9:
	s_waitcnt vmcnt(0)
	s_barrier
	s_cmp_lg_u32 s91, 0
	s_cbranch_scc1 .Lmy_b1a_done
	s_mov_b64 s[4:5], exec
	s_mov_b64 exec, 1
	v_readlane_b32 s6, v254, 36
	v_readlane_b32 s7, v254, 37
	v_readlane_b32 s8, v254, 21
	s_and_b32 s8, s8, 7
	s_lshl_b32 s9, s8, 8
	s_lshl_b32 s8, s8, 2
	s_add_u32 s10, s6, 0x1400
	s_addc_u32 s11, s7, 0
	v_mov_b32_e32 v0, s9
	v_mov_b32_e32 v48, 1
	global_atomic_add v48, v0, v48, s[10:11] sc0
	s_waitcnt vmcnt(0)
	v_readfirstlane_b32 s9, v48
	s_add_u32 s9, s9, 1
	s_cmp_lg_u32 s9, 32
	s_cbranch_scc1 .Lmy_b1a_rest
	buffer_wbl2 sc1
	v_mov_b32_e32 v0, s8
	v_mov_b32_e32 v48, 1
	s_waitcnt vmcnt(0)
	global_store_dword v0, v48, s[6:7] sc1
.Lmy_b1a_rest:
	s_mov_b64 exec, s[4:5]

; __device__ __forceinline__ unsigned xb_ld(unsigned* p)              { return __hip_atomic_load(p, __ATOMIC_RELAXED, __HIP_MEMORY_SCOPE_AGENT); }
; __device__ __forceinline__ unsigned xb_add(unsigned* p, unsigned v) { return __hip_atomic_fetch_add(p, v, __ATOMIC_RELAXED, __HIP_MEMORY_SCOPE_AGENT); }
; __device__ __forceinline__ void xcd_barrier_complete(unsigned* bar, unsigned x, unsigned& nloc, unsigned& nx) {
;     const unsigned G = gridDim.x * gridDim.y * gridDim.z;
;     unsigned sum, cnt, mine, sp = 0u;
;     for (;;) {
;         sum = 0u; cnt = 0u; mine = 0u;
; #pragma unroll
;         for (unsigned j = 0; j < 16; ++j) { const unsigned c = xb_ld(&bar[XB_XCNT(j)]); sum += c; cnt += (c > 0u) ? 1u : 0u; mine = (j == x) ? c : mine; }
;         if (sum == G) break;
;         __builtin_amdgcn_s_sleep(1);
;         if ((++sp & 255u) == 0u) { if (xb_ld(&bar[XB_TMO])) break; if (sp > XB_SPIN_CAP) { atomicAdd(&bar[XB_TMO], 1u); break; } }
;     }
;     nloc = mine > 0u ? mine : 1u; nx = cnt > 0u ? cnt : 1u;
; }
; __device__ __forceinline__ void xcd_barrier(const XcdBarrier& b, const int wave) {
;     asm volatile("s_waitcnt vmcnt(0)" ::: "memory");
;     __syncthreads();
;     if (phase_tid(wave) == 0) {
;         unsigned* bar = b.bar;
;         __builtin_amdgcn_s_waitcnt(0);
;         unsigned nloc = b.st[0], nx = b.st[1];
;         if (nloc == 0u) { xcd_barrier_complete(bar, b.x, nloc, nx); b.st[0] = nloc; b.st[1] = nx; }
;         const unsigned old = xb_add(&bar[XB_XSUB(b.x)], 1u);
;         const unsigned gen = old / nloc;
;         if (old + 1u == (gen + 1u) * nloc) {
;             __builtin_amdgcn_fence(__ATOMIC_RELEASE, "agent");
;             asm volatile("s_waitcnt vmcnt(0)" ::: "memory");
;             const unsigned og = xb_add(&bar[XB_TOP], 1u);
;             const unsigned tg = og / nx;
;             if (og + 1u == (tg + 1u) * nx) xb_add(&bar[XB_TOPGEN], 1u);
;             else XB_SPIN(xb_ld(&bar[XB_TOPGEN]) == tg, bar);
;             __builtin_amdgcn_fence(__ATOMIC_ACQUIRE, "agent");
;             xb_add(&bar[XB_XGEN(b.x)], 1u);
;             asm volatile("s_waitcnt vmcnt(0)" ::: "memory");
;         } else {
;             XB_SPIN(xb_ld(&bar[XB_XGEN(b.x)]) == gen, bar);
;             __builtin_amdgcn_fence(__ATOMIC_ACQUIRE, "agent");
;             asm volatile("s_waitcnt vmcnt(0)" ::: "memory");
;         }
;     }
;     __syncthreads();
; }
.LBB0_29:
	s_or_b64 exec, exec, s[0:1]
	s_waitcnt vmcnt(0)
	s_sub_i32 s0, 0, s91
	s_barrier
	v_mbcnt_lo_u32_b32 v0, -1, 0
	v_mbcnt_hi_u32_b32 v0, -1, v0
	v_writelane_b32 v255, s0, 25
	v_cmp_eq_u32_e32 vcc, s0, v0
	s_and_saveexec_b64 s[0:1], vcc
	v_writelane_b32 v255, s46, 26
	s_nop 1
	v_writelane_b32 v255, s47, 27
	v_writelane_b32 v255, s90, 28
	v_writelane_b32 v255, s91, 29
	s_cbranch_execz .LBB0_81
	v_readlane_b32 s30, v254, 36
	v_readlane_b32 s31, v254, 37
	s_nop 4
